# ntload
# speedup vs baseline: 1.0323x; 1.0211x over previous
.LBB0_23:
	s_and_b64 vcc, exec, s[4:5]
	s_cbranch_vccz .LBB0_358
	s_lshl_b32 s3, s2, 2
	s_addk_i32 s3, 0xf7a8
	v_lshrrev_b32_e32 v1, 6, v0
	v_or_b32_e32 v2, s3, v1
	s_load_dwordx4 s[12:15], s[0:1], 0x28
	s_load_dwordx2 s[4:5], s[0:1], 0x38
	v_ashrrev_i32_e32 v3, 31, v2
	v_and_b32_e32 v7, 63, v0
	v_lshlrev_b64 v[4:5], 7, v[2:3]
	v_or_b32_e32 v4, v4, v7
	v_lshlrev_b64 v[12:13], 2, v[4:5]
	s_waitcnt lgkmcnt(0)
	v_lshl_add_u64 v[8:9], s[12:13], 0, v[12:13]
	global_load_dword v10, v[8:9], off nt
	global_load_dword v11, v[8:9], off offset:256 nt
	v_lshl_add_u64 v[14:15], s[14:15], 0, v[12:13]
	v_lshl_add_u64 v[12:13], s[4:5], 0, v[12:13]
	global_load_dword v9, v[14:15], off nt
	global_load_dword v8, v[14:15], off offset:256 nt
	global_load_dword v1, v[12:13], off nt
	global_load_dword v6, v[12:13], off offset:256 nt
	s_mov_b32 s3, 0xbfb8aa3b
	s_waitcnt vmcnt(5)
	v_add_f32_e32 v10, 0xc1200000, v10
	v_mul_f32_e64 v12, |v10|, s3
	v_exp_f32_e32 v13, v12
	s_mov_b32 s3, 0x3c23d70a
	v_cmp_ngt_f32_e32 vcc, s3, v13
	s_and_saveexec_b64 s[4:5], vcc
	s_xor_b64 s[10:11], exec, s[4:5]
	s_cbranch_execz .LBB0_26
	v_add_f32_e32 v12, 1.0, v13
	s_mov_b32 s3, 0x800000
	v_cmp_gt_f32_e32 vcc, s3, v12
	s_mov_b32 s3, 0x3f317217
	s_nop 0
	v_cndmask_b32_e64 v13, 0, 32, vcc
	v_ldexp_f32 v12, v12, v13
	v_log_f32_e32 v12, v12
	s_nop 0
	v_mul_f32_e32 v13, 0x3f317217, v12
	v_fma_f32 v13, v12, s3, -v13
	v_fmamk_f32 v13, v12, 0x3377d1cf, v13
	s_mov_b32 s3, 0x7f800000
	v_fmac_f32_e32 v13, 0x3f317217, v12
	v_cmp_lt_f32_e64 s[4:5], |v12|, s3
	s_nop 1
	v_cndmask_b32_e64 v12, v12, v13, s[4:5]
	v_mov_b32_e32 v13, 0x41b17218
	v_cndmask_b32_e32 v13, 0, v13, vcc
	v_sub_f32_e32 v12, v12, v13
